# peeled first K-loop iteration with SrcC=0 (no accumulator zeroing v_movs) + nt epilogue stores
# speedup vs baseline: 1.2175x; 1.0028x over previous
.LBB0_310:
	s_ashr_i32 s91, s90, 31
	s_lshl_b64 s[4:5], s[90:91], 20
	s_add_u32 s62, s66, s4
	s_addc_u32 s63, s67, s5
	s_and_b64 s[4:5], s[36:37], exec
	s_cselect_b32 s4, s63, s25
	s_cselect_b32 s5, s62, s24
	s_ashr_i32 s89, s88, 31
	s_lshl_b64 s[20:21], s[88:89], 20
	s_add_u32 s20, s72, s20
	s_addc_u32 s21, s73, s21
	s_and_b64 s[30:31], s[36:37], exec
	s_cselect_b32 s8, s21, s1
	s_cselect_b32 s13, s20, s0
	s_add_u32 s17, s0, 0x10000
	s_addc_u32 s19, s1, 0
	s_add_u32 s0, s24, 0x80080
	s_addc_u32 s1, s25, 0
	s_mov_b32 s28, -2
	v_add_u32_e32 v100, s3, v190
	v_add_u32_e32 v156, s75, v190
	ds_read_b128 v[40:43], v100
	ds_read_b128 v[60:63], v100 offset:1024
	ds_read_b128 v[80:83], v100 offset:2048
	ds_read_b128 v[100:103], v100 offset:3072
	ds_read_b128 v[120:123], v156
	ds_read_b128 v[140:143], v156 offset:1024
	ds_read_b128 v[152:155], v156 offset:2048
	ds_read_b128 v[156:159], v156 offset:3072
	s_add_u32 s24, s0, 0xfff80080
	s_addc_u32 s25, s1, -1
	s_cmp_eq_u32 s28, 28
	s_cselect_b32 s39, s4, s25
	s_cselect_b32 s38, s5, s24
	s_cselect_b32 s25, s8, s19
	s_cselect_b32 s24, s13, s17
	v_lshl_add_u64 v[188:189], s[0:1], 0, v[168:169]
	s_add_i32 m0, s78, 0xc000
	ds_read_b128 v[172:175], v191
	ds_read_b128 v[176:179], v191 offset:1024
	ds_read_b128 v[180:183], v191 offset:2048
	ds_read_b128 v[184:187], v191 offset:3072
	ds_read_b128 v[192:195], v191 offset:4096
	ds_read_b128 v[196:199], v191 offset:5120
	ds_read_b128 v[200:203], v191 offset:6144
	ds_read_b128 v[204:207], v191 offset:7168
	global_load_lds_dwordx4 v[188:189], off
	v_lshl_add_u64 v[188:189], s[0:1], 0, v[170:171]
	s_add_i32 m0, s78, 0xe000
	s_nop 0
	global_load_lds_dwordx4 v[188:189], off
	s_waitcnt vmcnt(8)
	s_waitcnt lgkmcnt(0)
	s_barrier
	s_setprio 1
	s_waitcnt lgkmcnt(0)
	v_mfma_f32_16x16x32_bf16 v[148:151], v[40:43], v[172:175], 0
	v_mfma_f32_16x16x32_bf16 v[144:147], v[80:83], v[172:175], 0
	v_mfma_f32_16x16x32_bf16 v[128:131], v[40:43], v[180:183], 0
	v_mfma_f32_16x16x32_bf16 v[124:127], v[80:83], v[180:183], 0
	v_mfma_f32_16x16x32_bf16 v[108:111], v[40:43], v[192:195], 0
	v_mfma_f32_16x16x32_bf16 v[104:107], v[80:83], v[192:195], 0
	v_mfma_f32_16x16x32_bf16 v[88:91], v[40:43], v[200:203], 0
	v_mfma_f32_16x16x32_bf16 v[84:87], v[80:83], v[200:203], 0
	v_mfma_f32_16x16x32_bf16 v[148:151], v[60:63], v[176:179], v[148:151]
	v_mfma_f32_16x16x32_bf16 v[144:147], v[100:103], v[176:179], v[144:147]
	v_mfma_f32_16x16x32_bf16 v[128:131], v[60:63], v[184:187], v[128:131]
	v_mfma_f32_16x16x32_bf16 v[124:127], v[100:103], v[184:187], v[124:127]
	v_mfma_f32_16x16x32_bf16 v[108:111], v[60:63], v[196:199], v[108:111]
	v_mfma_f32_16x16x32_bf16 v[104:107], v[100:103], v[196:199], v[104:107]
	v_mfma_f32_16x16x32_bf16 v[88:91], v[60:63], v[204:207], v[88:91]
	v_mfma_f32_16x16x32_bf16 v[84:87], v[100:103], v[204:207], v[84:87]
	s_setprio 0
	s_setprio 1
	v_mfma_f32_16x16x32_bf16 v[136:139], v[120:123], v[172:175], 0
	v_mfma_f32_16x16x32_bf16 v[132:135], v[152:155], v[172:175], 0
	v_mfma_f32_16x16x32_bf16 v[116:119], v[120:123], v[180:183], 0
	v_mfma_f32_16x16x32_bf16 v[112:115], v[152:155], v[180:183], 0
	v_mfma_f32_16x16x32_bf16 v[96:99], v[120:123], v[192:195], 0
	v_mfma_f32_16x16x32_bf16 v[92:95], v[152:155], v[192:195], 0
	v_mfma_f32_16x16x32_bf16 v[76:79], v[120:123], v[200:203], 0
	v_mfma_f32_16x16x32_bf16 v[72:75], v[152:155], v[200:203], 0
	v_mfma_f32_16x16x32_bf16 v[136:139], v[140:143], v[176:179], v[136:139]
	v_mfma_f32_16x16x32_bf16 v[132:135], v[156:159], v[176:179], v[132:135]
	v_mfma_f32_16x16x32_bf16 v[116:119], v[140:143], v[184:187], v[116:119]
	v_mfma_f32_16x16x32_bf16 v[112:115], v[156:159], v[184:187], v[112:115]
	v_mfma_f32_16x16x32_bf16 v[96:99], v[140:143], v[196:199], v[96:99]
	v_mfma_f32_16x16x32_bf16 v[92:95], v[156:159], v[196:199], v[92:95]
	v_mfma_f32_16x16x32_bf16 v[76:79], v[140:143], v[204:207], v[76:79]
	v_mfma_f32_16x16x32_bf16 v[72:75], v[156:159], v[204:207], v[72:75]
	s_setprio 0
	s_barrier
	s_mov_b32 m0, s23
	v_lshl_add_u64 v[188:189], s[24:25], 0, v[162:163]
	s_add_u32 s30, s24, 0x4000
	ds_read_b128 v[172:175], v191 offset:16384
	ds_read_b128 v[176:179], v191 offset:17408
	ds_read_b128 v[180:183], v191 offset:18432
	ds_read_b128 v[184:187], v191 offset:19456
	ds_read_b128 v[192:195], v191 offset:20480
	ds_read_b128 v[196:199], v191 offset:21504
	ds_read_b128 v[200:203], v191 offset:22528
	ds_read_b128 v[204:207], v191 offset:23552
	global_load_lds_dwordx4 v[188:189], off
	v_lshl_add_u64 v[188:189], s[24:25], 0, v[166:167]
	s_mov_b32 m0, s74
	s_addc_u32 s31, s25, 0
	global_load_lds_dwordx4 v[188:189], off
	v_lshl_add_u64 v[188:189], s[30:31], 0, v[162:163]
	s_mov_b32 m0, s76
	v_lshl_add_u64 v[208:209], s[38:39], 0, v[164:165]
	global_load_lds_dwordx4 v[188:189], off
	v_lshl_add_u64 v[188:189], s[30:31], 0, v[166:167]
	s_mov_b32 m0, s77
	s_nop 0
	global_load_lds_dwordx4 v[188:189], off
	v_lshl_add_u64 v[188:189], s[38:39], 0, v[160:161]
	s_mov_b32 m0, s78
	s_nop 0
	global_load_lds_dwordx4 v[188:189], off
	s_mov_b32 m0, s79
	s_nop 0
	global_load_lds_dwordx4 v[208:209], off
	s_waitcnt vmcnt(8)
	s_waitcnt lgkmcnt(0)
	s_barrier
	s_setprio 1
	s_waitcnt lgkmcnt(0)
	v_mfma_f32_16x16x32_bf16 v[68:71], v[40:43], v[172:175], 0
	v_mfma_f32_16x16x32_bf16 v[64:67], v[80:83], v[172:175], 0
	v_mfma_f32_16x16x32_bf16 v[48:51], v[40:43], v[180:183], 0
	v_mfma_f32_16x16x32_bf16 v[44:47], v[80:83], v[180:183], 0
	v_mfma_f32_16x16x32_bf16 v[28:31], v[40:43], v[192:195], 0
	v_mfma_f32_16x16x32_bf16 v[24:27], v[80:83], v[192:195], 0
	v_mfma_f32_16x16x32_bf16 v[12:15], v[40:43], v[200:203], 0
	v_mfma_f32_16x16x32_bf16 v[8:11], v[80:83], v[200:203], 0
	v_mfma_f32_16x16x32_bf16 v[68:71], v[60:63], v[176:179], v[68:71]
	v_mfma_f32_16x16x32_bf16 v[64:67], v[100:103], v[176:179], v[64:67]
	v_mfma_f32_16x16x32_bf16 v[48:51], v[60:63], v[184:187], v[48:51]
	v_mfma_f32_16x16x32_bf16 v[44:47], v[100:103], v[184:187], v[44:47]
	v_mfma_f32_16x16x32_bf16 v[28:31], v[60:63], v[196:199], v[28:31]
	v_mfma_f32_16x16x32_bf16 v[24:27], v[100:103], v[196:199], v[24:27]
	v_mfma_f32_16x16x32_bf16 v[12:15], v[60:63], v[204:207], v[12:15]
	v_mfma_f32_16x16x32_bf16 v[8:11], v[100:103], v[204:207], v[8:11]
	s_setprio 0
	s_setprio 1
	v_mfma_f32_16x16x32_bf16 v[52:55], v[152:155], v[172:175], 0
	v_mfma_f32_16x16x32_bf16 v[36:39], v[120:123], v[180:183], 0
	v_mfma_f32_16x16x32_bf16 v[32:35], v[152:155], v[180:183], 0
	v_mfma_f32_16x16x32_bf16 v[20:23], v[120:123], v[192:195], 0
	v_mfma_f32_16x16x32_bf16 v[16:19], v[152:155], v[192:195], 0
	v_mfma_f32_16x16x32_bf16 v[4:7], v[120:123], v[200:203], 0
	v_mfma_f32_16x16x32_bf16 v[0:3], v[152:155], v[200:203], 0
	v_mfma_f32_16x16x32_bf16 v[40:43], v[120:123], v[172:175], 0
	v_mfma_f32_16x16x32_bf16 v[52:55], v[156:159], v[176:179], v[52:55]
	v_mfma_f32_16x16x32_bf16 v[36:39], v[140:143], v[184:187], v[36:39]
	v_mfma_f32_16x16x32_bf16 v[32:35], v[156:159], v[184:187], v[32:35]
	v_mfma_f32_16x16x32_bf16 v[20:23], v[140:143], v[196:199], v[20:23]
	v_mfma_f32_16x16x32_bf16 v[16:19], v[156:159], v[196:199], v[16:19]
	v_mfma_f32_16x16x32_bf16 v[4:7], v[140:143], v[204:207], v[4:7]
	v_mfma_f32_16x16x32_bf16 v[0:3], v[156:159], v[204:207], v[0:3]
	v_mfma_f32_16x16x32_bf16 v[40:43], v[140:143], v[176:179], v[40:43]
	s_setprio 0
	s_barrier
	v_add_u32_e32 v100, s86, v190
	v_add_u32_e32 v156, s95, v190
	ds_read_b128 v[56:59], v100
	ds_read_b128 v[60:63], v100 offset:1024
	ds_read_b128 v[80:83], v100 offset:2048
	ds_read_b128 v[100:103], v100 offset:3072
	ds_read_b128 v[120:123], v156
	ds_read_b128 v[140:143], v156 offset:1024
	ds_read_b128 v[152:155], v156 offset:2048
	ds_read_b128 v[156:159], v156 offset:3072
	s_add_u32 s30, s38, 0x80000
	s_addc_u32 s31, s39, 0
	s_mov_b32 m0, s82
	v_lshl_add_u64 v[210:211], s[30:31], 0, v[160:161]
	ds_read_b128 v[172:175], v191 offset:32768
	ds_read_b128 v[176:179], v191 offset:33792
	ds_read_b128 v[180:183], v191 offset:34816
	ds_read_b128 v[184:187], v191 offset:35840
	ds_read_b128 v[192:195], v191 offset:36864
	ds_read_b128 v[196:199], v191 offset:37888
	ds_read_b128 v[200:203], v191 offset:38912
	ds_read_b128 v[204:207], v191 offset:39936
	global_load_lds_dwordx4 v[210:211], off
	v_lshl_add_u64 v[210:211], s[30:31], 0, v[164:165]
	s_mov_b32 m0, s83
	s_nop 0
	global_load_lds_dwordx4 v[210:211], off
	s_waitcnt vmcnt(8)
	s_waitcnt lgkmcnt(0)
	s_barrier
	s_setprio 1
	s_waitcnt lgkmcnt(0)
	v_mfma_f32_16x16x32_bf16 v[148:151], v[56:59], v[172:175], v[148:151]
	v_mfma_f32_16x16x32_bf16 v[144:147], v[80:83], v[172:175], v[144:147]
	v_mfma_f32_16x16x32_bf16 v[128:131], v[56:59], v[180:183], v[128:131]
	v_mfma_f32_16x16x32_bf16 v[124:127], v[80:83], v[180:183], v[124:127]
	v_mfma_f32_16x16x32_bf16 v[108:111], v[56:59], v[192:195], v[108:111]
	v_mfma_f32_16x16x32_bf16 v[104:107], v[80:83], v[192:195], v[104:107]
	v_mfma_f32_16x16x32_bf16 v[88:91], v[56:59], v[200:203], v[88:91]
	v_mfma_f32_16x16x32_bf16 v[84:87], v[80:83], v[200:203], v[84:87]
	v_mfma_f32_16x16x32_bf16 v[148:151], v[60:63], v[176:179], v[148:151]
	v_mfma_f32_16x16x32_bf16 v[144:147], v[100:103], v[176:179], v[144:147]
	v_mfma_f32_16x16x32_bf16 v[128:131], v[60:63], v[184:187], v[128:131]
	v_mfma_f32_16x16x32_bf16 v[124:127], v[100:103], v[184:187], v[124:127]
	v_mfma_f32_16x16x32_bf16 v[108:111], v[60:63], v[196:199], v[108:111]
	v_mfma_f32_16x16x32_bf16 v[104:107], v[100:103], v[196:199], v[104:107]
	v_mfma_f32_16x16x32_bf16 v[88:91], v[60:63], v[204:207], v[88:91]
	v_mfma_f32_16x16x32_bf16 v[84:87], v[100:103], v[204:207], v[84:87]
	s_setprio 0
	s_setprio 1
	v_mfma_f32_16x16x32_bf16 v[136:139], v[120:123], v[172:175], v[136:139]
	v_mfma_f32_16x16x32_bf16 v[132:135], v[152:155], v[172:175], v[132:135]
	v_mfma_f32_16x16x32_bf16 v[116:119], v[120:123], v[180:183], v[116:119]
	v_mfma_f32_16x16x32_bf16 v[112:115], v[152:155], v[180:183], v[112:115]
	v_mfma_f32_16x16x32_bf16 v[96:99], v[120:123], v[192:195], v[96:99]
	v_mfma_f32_16x16x32_bf16 v[92:95], v[152:155], v[192:195], v[92:95]
	v_mfma_f32_16x16x32_bf16 v[76:79], v[120:123], v[200:203], v[76:79]
	v_mfma_f32_16x16x32_bf16 v[72:75], v[152:155], v[200:203], v[72:75]
	v_mfma_f32_16x16x32_bf16 v[136:139], v[140:143], v[176:179], v[136:139]
	v_mfma_f32_16x16x32_bf16 v[132:135], v[156:159], v[176:179], v[132:135]
	v_mfma_f32_16x16x32_bf16 v[116:119], v[140:143], v[184:187], v[116:119]
	v_mfma_f32_16x16x32_bf16 v[112:115], v[156:159], v[184:187], v[112:115]
	v_mfma_f32_16x16x32_bf16 v[96:99], v[140:143], v[196:199], v[96:99]
	v_mfma_f32_16x16x32_bf16 v[92:95], v[156:159], v[196:199], v[92:95]
	v_mfma_f32_16x16x32_bf16 v[76:79], v[140:143], v[204:207], v[76:79]
	v_mfma_f32_16x16x32_bf16 v[72:75], v[156:159], v[204:207], v[72:75]
	s_setprio 0
	s_barrier
	s_add_u32 s30, s24, 0x8000
	s_addc_u32 s31, s25, 0
	s_mov_b32 m0, s87
	v_lshl_add_u64 v[210:211], s[30:31], 0, v[162:163]
	s_add_u32 s24, s24, 0xc000
	ds_read_b128 v[172:175], v191 offset:49152
	ds_read_b128 v[176:179], v191 offset:50176
	ds_read_b128 v[180:183], v191 offset:51200
	ds_read_b128 v[184:187], v191 offset:52224
	ds_read_b128 v[192:195], v191 offset:53248
	ds_read_b128 v[196:199], v191 offset:54272
	ds_read_b128 v[200:203], v191 offset:55296
	ds_read_b128 v[204:207], v191 offset:56320
	global_load_lds_dwordx4 v[210:211], off
	v_lshl_add_u64 v[210:211], s[30:31], 0, v[166:167]
	s_mov_b32 m0, s92
	s_addc_u32 s25, s25, 0
	global_load_lds_dwordx4 v[210:211], off
	v_lshl_add_u64 v[210:211], s[24:25], 0, v[162:163]
	s_mov_b32 m0, s96
	v_lshl_add_u64 v[188:189], v[188:189], 0, s[26:27]
	global_load_lds_dwordx4 v[210:211], off
	v_lshl_add_u64 v[210:211], s[24:25], 0, v[166:167]
	s_mov_b32 m0, s97
	s_nop 0
	global_load_lds_dwordx4 v[210:211], off
	s_mov_b32 m0, s93
	s_nop 0
	global_load_lds_dwordx4 v[188:189], off
	v_lshl_add_u64 v[188:189], v[208:209], 0, s[26:27]
	s_mov_b32 m0, s94
	s_nop 0
	global_load_lds_dwordx4 v[188:189], off
	s_waitcnt vmcnt(8)
	s_waitcnt lgkmcnt(0)
	s_barrier
	s_setprio 1
	s_waitcnt lgkmcnt(0)
	v_mfma_f32_16x16x32_bf16 v[68:71], v[56:59], v[172:175], v[68:71]
	v_mfma_f32_16x16x32_bf16 v[64:67], v[80:83], v[172:175], v[64:67]
	v_mfma_f32_16x16x32_bf16 v[48:51], v[56:59], v[180:183], v[48:51]
	v_mfma_f32_16x16x32_bf16 v[44:47], v[80:83], v[180:183], v[44:47]
	v_mfma_f32_16x16x32_bf16 v[28:31], v[56:59], v[192:195], v[28:31]
	v_mfma_f32_16x16x32_bf16 v[24:27], v[80:83], v[192:195], v[24:27]
	v_mfma_f32_16x16x32_bf16 v[12:15], v[56:59], v[200:203], v[12:15]
	v_mfma_f32_16x16x32_bf16 v[8:11], v[80:83], v[200:203], v[8:11]
	v_mfma_f32_16x16x32_bf16 v[68:71], v[60:63], v[176:179], v[68:71]
	v_mfma_f32_16x16x32_bf16 v[64:67], v[100:103], v[176:179], v[64:67]
	v_mfma_f32_16x16x32_bf16 v[48:51], v[60:63], v[184:187], v[48:51]
	v_mfma_f32_16x16x32_bf16 v[44:47], v[100:103], v[184:187], v[44:47]
	v_mfma_f32_16x16x32_bf16 v[28:31], v[60:63], v[196:199], v[28:31]
	v_mfma_f32_16x16x32_bf16 v[24:27], v[100:103], v[196:199], v[24:27]
	v_mfma_f32_16x16x32_bf16 v[12:15], v[60:63], v[204:207], v[12:15]
	v_mfma_f32_16x16x32_bf16 v[8:11], v[100:103], v[204:207], v[8:11]
	s_setprio 0
	s_setprio 1
	v_mfma_f32_16x16x32_bf16 v[40:43], v[120:123], v[172:175], v[40:43]
	v_mfma_f32_16x16x32_bf16 v[56:59], v[140:143], v[176:179], v[40:43]
	v_mfma_f32_16x16x32_bf16 v[40:43], v[152:155], v[172:175], v[52:55]
	v_mfma_f32_16x16x32_bf16 v[36:39], v[120:123], v[180:183], v[36:39]
	v_mfma_f32_16x16x32_bf16 v[32:35], v[152:155], v[180:183], v[32:35]
	v_mfma_f32_16x16x32_bf16 v[20:23], v[120:123], v[192:195], v[20:23]
	v_mfma_f32_16x16x32_bf16 v[16:19], v[152:155], v[192:195], v[16:19]
	v_mfma_f32_16x16x32_bf16 v[4:7], v[120:123], v[200:203], v[4:7]
	v_mfma_f32_16x16x32_bf16 v[0:3], v[152:155], v[200:203], v[0:3]
	v_mfma_f32_16x16x32_bf16 v[52:55], v[156:159], v[176:179], v[40:43]
	v_mfma_f32_16x16x32_bf16 v[36:39], v[140:143], v[184:187], v[36:39]
	v_mfma_f32_16x16x32_bf16 v[32:35], v[156:159], v[184:187], v[32:35]
	v_mfma_f32_16x16x32_bf16 v[20:23], v[140:143], v[196:199], v[20:23]
	v_mfma_f32_16x16x32_bf16 v[16:19], v[156:159], v[196:199], v[16:19]
	v_mfma_f32_16x16x32_bf16 v[4:7], v[140:143], v[204:207], v[4:7]
	v_mfma_f32_16x16x32_bf16 v[0:3], v[156:159], v[204:207], v[0:3]
	s_setprio 0
	s_barrier
	s_add_i32 s28, s28, 2
	s_add_u32 s17, s17, 0x10000
	s_addc_u32 s19, s19, 0
	s_add_u32 s0, s0, 0x100
	s_addc_u32 s1, s1, 0
	s_cmp_gt_u32 s28, 29

.LBB0_618:
	v_readlane_b32 s0, v253, 42
	v_readlane_b32 s1, v253, 43
	s_andn2_b64 vcc, exec, s[0:1]
	s_cbranch_vccnz .LBB0_668
	s_mov_b32 s0, -1
	s_waitcnt vmcnt(0)
	s_nop 0
	v_mbcnt_lo_u32_b32 v0, s0, 0
	v_mbcnt_hi_u32_b32 v0, s0, v0
	v_readlane_b32 s0, v253, 50
	s_barrier
	s_nop 0
	v_cmp_eq_u32_e32 vcc, s0, v0
	s_and_saveexec_b64 s[0:1], vcc
	s_cbranch_execz .LBB0_667
	v_readlane_b32 s2, v253, 44
	s_waitcnt vmcnt(0) expcnt(0) lgkmcnt(0)
	s_nop 0
	v_mov_b32_e32 v0, s2
	ds_read_b32 v2, v0
	ds_read_b32 v0, v0 offset:4
	s_waitcnt lgkmcnt(1)
	v_cmp_ne_u32_e32 vcc, 0, v2
	s_cbranch_vccnz .LBB0_635
	v_readlane_b32 s4, v253, 47
	v_readlane_b32 s5, v253, 48
	s_load_dwordx2 s[2:3], s[4:5], 0x0
	s_nop 0
	s_load_dword s4, s[4:5], 0x8
	s_mov_b32 s13, 1
	s_waitcnt lgkmcnt(0)
	s_mul_i32 s8, s3, s2
	s_mul_i32 s8, s8, s4
	s_branch .LBB0_623
.Ltramp_214:
	s_branch .LBB0_214
.Ltramp_213:
	s_branch .LBB0_213
.LBB0_622:
	s_and_b64 vcc, exec, s[4:5]
	s_cbranch_vccnz .LBB0_630

.LBB0_1054:
	s_ashr_i32 s41, s40, 31
	s_lshl_b64 s[4:5], s[40:41], 20
	s_add_u32 s44, s16, s4
	s_addc_u32 s45, s17, s5
	s_and_b64 s[4:5], s[36:37], exec
	s_cselect_b32 s4, s45, s51
	s_cselect_b32 s5, s44, s50
	s_ashr_i32 s39, s38, 31
	s_lshl_b64 s[46:47], s[38:39], 20
	s_add_u32 s46, s18, s46
	s_addc_u32 s47, s19, s47
	s_and_b64 s[52:53], s[36:37], exec
	s_cselect_b32 s39, s47, s1
	s_cselect_b32 s41, s46, s0
	s_add_u32 s49, s0, 0x10000
	s_addc_u32 s55, s1, 0
	s_add_u32 s0, s50, 0x80080
	s_addc_u32 s1, s51, 0
	s_mov_b32 s80, -2
	v_add_u32_e32 v140, s28, v215
	v_add_u32_e32 v156, s54, v215
	ds_read_b128 v[128:131], v140
	ds_read_b128 v[132:135], v140 offset:1024
	ds_read_b128 v[136:139], v140 offset:2048
	ds_read_b128 v[140:143], v140 offset:3072
	ds_read_b128 v[144:147], v156
	ds_read_b128 v[148:151], v156 offset:1024
	ds_read_b128 v[152:155], v156 offset:2048
	ds_read_b128 v[156:159], v156 offset:3072
	s_add_u32 s50, s0, 0xfff80080
	s_addc_u32 s51, s1, -1
	s_cmp_eq_u32 s80, 28
	s_cselect_b32 s53, s4, s51
	s_cselect_b32 s52, s5, s50
	s_cselect_b32 s51, s39, s55
	s_cselect_b32 s50, s41, s49
	v_lshl_add_u64 v[204:205], s[0:1], 0, v[180:181]
	s_add_i32 m0, s58, 0xc000
	ds_read_b128 v[160:163], v251
	ds_read_b128 v[164:167], v251 offset:1024
	ds_read_b128 v[168:171], v251 offset:2048
	ds_read_b128 v[184:187], v251 offset:3072
	ds_read_b128 v[188:191], v251 offset:4096
	ds_read_b128 v[192:195], v251 offset:5120
	ds_read_b128 v[196:199], v251 offset:6144
	ds_read_b128 v[200:203], v251 offset:7168
	global_load_lds_dwordx4 v[204:205], off
	v_lshl_add_u64 v[204:205], s[0:1], 0, v[182:183]
	s_add_i32 m0, s58, 0xe000
	s_nop 0
	global_load_lds_dwordx4 v[204:205], off
	s_waitcnt vmcnt(8)
	s_waitcnt lgkmcnt(0)
	s_barrier
	s_setprio 1
	s_waitcnt lgkmcnt(0)
	v_mfma_f32_16x16x32_bf16 v[124:127], v[128:131], v[160:163], 0
	v_mfma_f32_16x16x32_bf16 v[120:123], v[136:139], v[160:163], 0
	v_mfma_f32_16x16x32_bf16 v[116:119], v[128:131], v[168:171], 0
	v_mfma_f32_16x16x32_bf16 v[112:115], v[136:139], v[168:171], 0
	v_mfma_f32_16x16x32_bf16 v[108:111], v[128:131], v[188:191], 0
	v_mfma_f32_16x16x32_bf16 v[104:107], v[136:139], v[188:191], 0
	v_mfma_f32_16x16x32_bf16 v[100:103], v[128:131], v[196:199], 0
	v_mfma_f32_16x16x32_bf16 v[96:99], v[136:139], v[196:199], 0
	v_mfma_f32_16x16x32_bf16 v[124:127], v[132:135], v[164:167], v[124:127]
	v_mfma_f32_16x16x32_bf16 v[120:123], v[140:143], v[164:167], v[120:123]
	v_mfma_f32_16x16x32_bf16 v[116:119], v[132:135], v[184:187], v[116:119]
	v_mfma_f32_16x16x32_bf16 v[112:115], v[140:143], v[184:187], v[112:115]
	v_mfma_f32_16x16x32_bf16 v[108:111], v[132:135], v[192:195], v[108:111]
	v_mfma_f32_16x16x32_bf16 v[104:107], v[140:143], v[192:195], v[104:107]
	v_mfma_f32_16x16x32_bf16 v[100:103], v[132:135], v[200:203], v[100:103]
	v_mfma_f32_16x16x32_bf16 v[96:99], v[140:143], v[200:203], v[96:99]
	s_setprio 0
	s_setprio 1
	v_mfma_f32_16x16x32_bf16 v[60:63], v[144:147], v[160:163], 0
	v_mfma_f32_16x16x32_bf16 v[56:59], v[152:155], v[160:163], 0
	v_mfma_f32_16x16x32_bf16 v[52:55], v[144:147], v[168:171], 0
	v_mfma_f32_16x16x32_bf16 v[48:51], v[152:155], v[168:171], 0
	v_mfma_f32_16x16x32_bf16 v[44:47], v[144:147], v[188:191], 0
	v_mfma_f32_16x16x32_bf16 v[40:43], v[152:155], v[188:191], 0
	v_mfma_f32_16x16x32_bf16 v[36:39], v[144:147], v[196:199], 0
	v_mfma_f32_16x16x32_bf16 v[32:35], v[152:155], v[196:199], 0
	v_mfma_f32_16x16x32_bf16 v[60:63], v[148:151], v[164:167], v[60:63]
	v_mfma_f32_16x16x32_bf16 v[56:59], v[156:159], v[164:167], v[56:59]
	v_mfma_f32_16x16x32_bf16 v[52:55], v[148:151], v[184:187], v[52:55]
	v_mfma_f32_16x16x32_bf16 v[48:51], v[156:159], v[184:187], v[48:51]
	v_mfma_f32_16x16x32_bf16 v[44:47], v[148:151], v[192:195], v[44:47]
	v_mfma_f32_16x16x32_bf16 v[40:43], v[156:159], v[192:195], v[40:43]
	v_mfma_f32_16x16x32_bf16 v[36:39], v[148:151], v[200:203], v[36:39]
	v_mfma_f32_16x16x32_bf16 v[32:35], v[156:159], v[200:203], v[32:35]
	s_setprio 0
	s_barrier
	s_mov_b32 m0, s30
	v_lshl_add_u64 v[204:205], s[50:51], 0, v[174:175]
	s_add_u32 s82, s50, 0x4000
	ds_read_b128 v[160:163], v251 offset:16384
	ds_read_b128 v[164:167], v251 offset:17408
	ds_read_b128 v[168:171], v251 offset:18432
	ds_read_b128 v[184:187], v251 offset:19456
	ds_read_b128 v[188:191], v251 offset:20480
	ds_read_b128 v[192:195], v251 offset:21504
	ds_read_b128 v[196:199], v251 offset:22528
	ds_read_b128 v[200:203], v251 offset:23552
	global_load_lds_dwordx4 v[204:205], off
	v_lshl_add_u64 v[204:205], s[50:51], 0, v[178:179]
	s_mov_b32 m0, s43
	s_addc_u32 s83, s51, 0
	global_load_lds_dwordx4 v[204:205], off
	v_lshl_add_u64 v[204:205], s[82:83], 0, v[174:175]
	s_mov_b32 m0, s56
	v_lshl_add_u64 v[206:207], s[52:53], 0, v[176:177]
	global_load_lds_dwordx4 v[204:205], off
	v_lshl_add_u64 v[204:205], s[82:83], 0, v[178:179]
	s_mov_b32 m0, s57
	s_nop 0
	global_load_lds_dwordx4 v[204:205], off
	v_lshl_add_u64 v[204:205], s[52:53], 0, v[172:173]
	s_mov_b32 m0, s58
	s_nop 0
	global_load_lds_dwordx4 v[204:205], off
	s_mov_b32 m0, s59
	s_nop 0
	global_load_lds_dwordx4 v[206:207], off
	s_waitcnt vmcnt(8)
	s_waitcnt lgkmcnt(0)
	s_barrier
	s_setprio 1
	s_waitcnt lgkmcnt(0)
	v_mfma_f32_16x16x32_bf16 v[92:95], v[128:131], v[160:163], 0
	v_mfma_f32_16x16x32_bf16 v[88:91], v[136:139], v[160:163], 0
	v_mfma_f32_16x16x32_bf16 v[84:87], v[128:131], v[168:171], 0
	v_mfma_f32_16x16x32_bf16 v[80:83], v[136:139], v[168:171], 0
	v_mfma_f32_16x16x32_bf16 v[76:79], v[128:131], v[188:191], 0
	v_mfma_f32_16x16x32_bf16 v[72:75], v[136:139], v[188:191], 0
	v_mfma_f32_16x16x32_bf16 v[68:71], v[128:131], v[196:199], 0
	v_mfma_f32_16x16x32_bf16 v[64:67], v[136:139], v[196:199], 0
	v_mfma_f32_16x16x32_bf16 v[92:95], v[132:135], v[164:167], v[92:95]
	v_mfma_f32_16x16x32_bf16 v[88:91], v[140:143], v[164:167], v[88:91]
	v_mfma_f32_16x16x32_bf16 v[84:87], v[132:135], v[184:187], v[84:87]
	v_mfma_f32_16x16x32_bf16 v[80:83], v[140:143], v[184:187], v[80:83]
	v_mfma_f32_16x16x32_bf16 v[76:79], v[132:135], v[192:195], v[76:79]
	v_mfma_f32_16x16x32_bf16 v[72:75], v[140:143], v[192:195], v[72:75]
	v_mfma_f32_16x16x32_bf16 v[68:71], v[132:135], v[200:203], v[68:71]
	v_mfma_f32_16x16x32_bf16 v[64:67], v[140:143], v[200:203], v[64:67]
	s_setprio 0
	s_setprio 1
	v_mfma_f32_16x16x32_bf16 v[28:31], v[144:147], v[160:163], 0
	v_mfma_f32_16x16x32_bf16 v[24:27], v[152:155], v[160:163], 0
	v_mfma_f32_16x16x32_bf16 v[20:23], v[144:147], v[168:171], 0
	v_mfma_f32_16x16x32_bf16 v[16:19], v[152:155], v[168:171], 0
	v_mfma_f32_16x16x32_bf16 v[12:15], v[144:147], v[188:191], 0
	v_mfma_f32_16x16x32_bf16 v[8:11], v[152:155], v[188:191], 0
	v_mfma_f32_16x16x32_bf16 v[4:7], v[144:147], v[196:199], 0
	v_mfma_f32_16x16x32_bf16 v[0:3], v[152:155], v[196:199], 0
	v_mfma_f32_16x16x32_bf16 v[28:31], v[148:151], v[164:167], v[28:31]
	v_mfma_f32_16x16x32_bf16 v[24:27], v[156:159], v[164:167], v[24:27]
	v_mfma_f32_16x16x32_bf16 v[20:23], v[148:151], v[184:187], v[20:23]
	v_mfma_f32_16x16x32_bf16 v[16:19], v[156:159], v[184:187], v[16:19]
	v_mfma_f32_16x16x32_bf16 v[12:15], v[148:151], v[192:195], v[12:15]
	v_mfma_f32_16x16x32_bf16 v[8:11], v[156:159], v[192:195], v[8:11]
	v_mfma_f32_16x16x32_bf16 v[4:7], v[148:151], v[200:203], v[4:7]
	v_mfma_f32_16x16x32_bf16 v[0:3], v[156:159], v[200:203], v[0:3]
	s_setprio 0
	s_barrier
	v_add_u32_e32 v140, s68, v215
	v_add_u32_e32 v156, s73, v215
	ds_read_b128 v[128:131], v140
	ds_read_b128 v[132:135], v140 offset:1024
	ds_read_b128 v[136:139], v140 offset:2048
	ds_read_b128 v[140:143], v140 offset:3072
	ds_read_b128 v[144:147], v156
	ds_read_b128 v[148:151], v156 offset:1024
	ds_read_b128 v[152:155], v156 offset:2048
	ds_read_b128 v[156:159], v156 offset:3072
	s_add_u32 s52, s52, 0x80000
	s_addc_u32 s53, s53, 0
	s_mov_b32 m0, s60
	v_lshl_add_u64 v[208:209], s[52:53], 0, v[172:173]
	ds_read_b128 v[160:163], v251 offset:32768
	ds_read_b128 v[164:167], v251 offset:33792
	ds_read_b128 v[168:171], v251 offset:34816
	ds_read_b128 v[184:187], v251 offset:35840
	ds_read_b128 v[188:191], v251 offset:36864
	ds_read_b128 v[192:195], v251 offset:37888
	ds_read_b128 v[196:199], v251 offset:38912
	ds_read_b128 v[200:203], v251 offset:39936
	global_load_lds_dwordx4 v[208:209], off
	v_lshl_add_u64 v[208:209], s[52:53], 0, v[176:177]
	s_mov_b32 m0, s61
	s_nop 0
	global_load_lds_dwordx4 v[208:209], off
	s_waitcnt vmcnt(8)
	s_waitcnt lgkmcnt(0)
	s_barrier
	s_setprio 1
	s_waitcnt lgkmcnt(0)
	v_mfma_f32_16x16x32_bf16 v[124:127], v[128:131], v[160:163], v[124:127]
	v_mfma_f32_16x16x32_bf16 v[120:123], v[136:139], v[160:163], v[120:123]
	v_mfma_f32_16x16x32_bf16 v[116:119], v[128:131], v[168:171], v[116:119]
	v_mfma_f32_16x16x32_bf16 v[112:115], v[136:139], v[168:171], v[112:115]
	v_mfma_f32_16x16x32_bf16 v[108:111], v[128:131], v[188:191], v[108:111]
	v_mfma_f32_16x16x32_bf16 v[104:107], v[136:139], v[188:191], v[104:107]
	v_mfma_f32_16x16x32_bf16 v[100:103], v[128:131], v[196:199], v[100:103]
	v_mfma_f32_16x16x32_bf16 v[96:99], v[136:139], v[196:199], v[96:99]
	v_mfma_f32_16x16x32_bf16 v[124:127], v[132:135], v[164:167], v[124:127]
	v_mfma_f32_16x16x32_bf16 v[120:123], v[140:143], v[164:167], v[120:123]
	v_mfma_f32_16x16x32_bf16 v[116:119], v[132:135], v[184:187], v[116:119]
	v_mfma_f32_16x16x32_bf16 v[112:115], v[140:143], v[184:187], v[112:115]
	v_mfma_f32_16x16x32_bf16 v[108:111], v[132:135], v[192:195], v[108:111]
	v_mfma_f32_16x16x32_bf16 v[104:107], v[140:143], v[192:195], v[104:107]
	v_mfma_f32_16x16x32_bf16 v[100:103], v[132:135], v[200:203], v[100:103]
	v_mfma_f32_16x16x32_bf16 v[96:99], v[140:143], v[200:203], v[96:99]
	s_setprio 0
	s_setprio 1
	v_mfma_f32_16x16x32_bf16 v[60:63], v[144:147], v[160:163], v[60:63]
	v_mfma_f32_16x16x32_bf16 v[56:59], v[152:155], v[160:163], v[56:59]
	v_mfma_f32_16x16x32_bf16 v[52:55], v[144:147], v[168:171], v[52:55]
	v_mfma_f32_16x16x32_bf16 v[48:51], v[152:155], v[168:171], v[48:51]
	v_mfma_f32_16x16x32_bf16 v[44:47], v[144:147], v[188:191], v[44:47]
	v_mfma_f32_16x16x32_bf16 v[40:43], v[152:155], v[188:191], v[40:43]
	v_mfma_f32_16x16x32_bf16 v[36:39], v[144:147], v[196:199], v[36:39]
	v_mfma_f32_16x16x32_bf16 v[32:35], v[152:155], v[196:199], v[32:35]
	v_mfma_f32_16x16x32_bf16 v[60:63], v[148:151], v[164:167], v[60:63]
	v_mfma_f32_16x16x32_bf16 v[56:59], v[156:159], v[164:167], v[56:59]
	v_mfma_f32_16x16x32_bf16 v[52:55], v[148:151], v[184:187], v[52:55]
	v_mfma_f32_16x16x32_bf16 v[48:51], v[156:159], v[184:187], v[48:51]
	v_mfma_f32_16x16x32_bf16 v[44:47], v[148:151], v[192:195], v[44:47]
	v_mfma_f32_16x16x32_bf16 v[40:43], v[156:159], v[192:195], v[40:43]
	v_mfma_f32_16x16x32_bf16 v[36:39], v[148:151], v[200:203], v[36:39]
	v_mfma_f32_16x16x32_bf16 v[32:35], v[156:159], v[200:203], v[32:35]
	s_setprio 0
	s_barrier
	s_add_u32 s52, s50, 0x8000
	s_addc_u32 s53, s51, 0
	s_mov_b32 m0, s69
	v_lshl_add_u64 v[208:209], s[52:53], 0, v[174:175]
	s_add_u32 s50, s50, 0xc000
	ds_read_b128 v[160:163], v251 offset:49152
	ds_read_b128 v[164:167], v251 offset:50176
	ds_read_b128 v[168:171], v251 offset:51200
	ds_read_b128 v[184:187], v251 offset:52224
	ds_read_b128 v[188:191], v251 offset:53248
	ds_read_b128 v[192:195], v251 offset:54272
	ds_read_b128 v[196:199], v251 offset:55296
	ds_read_b128 v[200:203], v251 offset:56320
	global_load_lds_dwordx4 v[208:209], off
	v_lshl_add_u64 v[208:209], s[52:53], 0, v[178:179]
	s_mov_b32 m0, s70
	s_addc_u32 s51, s51, 0
	global_load_lds_dwordx4 v[208:209], off
	v_lshl_add_u64 v[208:209], s[50:51], 0, v[174:175]
	s_mov_b32 m0, s74
	v_lshl_add_u64 v[204:205], v[204:205], 0, s[26:27]
	global_load_lds_dwordx4 v[208:209], off
	v_lshl_add_u64 v[208:209], s[50:51], 0, v[178:179]
	s_mov_b32 m0, s75
	s_nop 0
	global_load_lds_dwordx4 v[208:209], off
	s_mov_b32 m0, s71
	s_nop 0
	global_load_lds_dwordx4 v[204:205], off
	v_lshl_add_u64 v[204:205], v[206:207], 0, s[26:27]
	s_mov_b32 m0, s72
	s_nop 0
	global_load_lds_dwordx4 v[204:205], off
	s_waitcnt vmcnt(8)
	s_waitcnt lgkmcnt(0)
	s_barrier
	s_setprio 1
	s_waitcnt lgkmcnt(0)
	v_mfma_f32_16x16x32_bf16 v[92:95], v[128:131], v[160:163], v[92:95]
	v_mfma_f32_16x16x32_bf16 v[88:91], v[136:139], v[160:163], v[88:91]
	v_mfma_f32_16x16x32_bf16 v[84:87], v[128:131], v[168:171], v[84:87]
	v_mfma_f32_16x16x32_bf16 v[80:83], v[136:139], v[168:171], v[80:83]
	v_mfma_f32_16x16x32_bf16 v[76:79], v[128:131], v[188:191], v[76:79]
	v_mfma_f32_16x16x32_bf16 v[72:75], v[136:139], v[188:191], v[72:75]
	v_mfma_f32_16x16x32_bf16 v[68:71], v[128:131], v[196:199], v[68:71]
	v_mfma_f32_16x16x32_bf16 v[64:67], v[136:139], v[196:199], v[64:67]
	v_mfma_f32_16x16x32_bf16 v[92:95], v[132:135], v[164:167], v[92:95]
	v_mfma_f32_16x16x32_bf16 v[88:91], v[140:143], v[164:167], v[88:91]
	v_mfma_f32_16x16x32_bf16 v[84:87], v[132:135], v[184:187], v[84:87]
	v_mfma_f32_16x16x32_bf16 v[80:83], v[140:143], v[184:187], v[80:83]
	v_mfma_f32_16x16x32_bf16 v[76:79], v[132:135], v[192:195], v[76:79]
	v_mfma_f32_16x16x32_bf16 v[72:75], v[140:143], v[192:195], v[72:75]
	v_mfma_f32_16x16x32_bf16 v[68:71], v[132:135], v[200:203], v[68:71]
	v_mfma_f32_16x16x32_bf16 v[64:67], v[140:143], v[200:203], v[64:67]
	s_setprio 0
	s_setprio 1
	v_mfma_f32_16x16x32_bf16 v[28:31], v[144:147], v[160:163], v[28:31]
	v_mfma_f32_16x16x32_bf16 v[24:27], v[152:155], v[160:163], v[24:27]
	v_mfma_f32_16x16x32_bf16 v[20:23], v[144:147], v[168:171], v[20:23]
	v_mfma_f32_16x16x32_bf16 v[16:19], v[152:155], v[168:171], v[16:19]
	v_mfma_f32_16x16x32_bf16 v[12:15], v[144:147], v[188:191], v[12:15]
	v_mfma_f32_16x16x32_bf16 v[8:11], v[152:155], v[188:191], v[8:11]
	v_mfma_f32_16x16x32_bf16 v[4:7], v[144:147], v[196:199], v[4:7]
	v_mfma_f32_16x16x32_bf16 v[0:3], v[152:155], v[196:199], v[0:3]
	v_mfma_f32_16x16x32_bf16 v[28:31], v[148:151], v[164:167], v[28:31]
	v_mfma_f32_16x16x32_bf16 v[24:27], v[156:159], v[164:167], v[24:27]
	v_mfma_f32_16x16x32_bf16 v[20:23], v[148:151], v[184:187], v[20:23]
	v_mfma_f32_16x16x32_bf16 v[16:19], v[156:159], v[184:187], v[16:19]
	v_mfma_f32_16x16x32_bf16 v[12:15], v[148:151], v[192:195], v[12:15]
	v_mfma_f32_16x16x32_bf16 v[8:11], v[156:159], v[192:195], v[8:11]
	v_mfma_f32_16x16x32_bf16 v[4:7], v[148:151], v[200:203], v[4:7]
	v_mfma_f32_16x16x32_bf16 v[0:3], v[156:159], v[200:203], v[0:3]
	s_setprio 0
	s_barrier
	s_add_i32 s80, s80, 2
	s_add_u32 s49, s49, 0x10000
	s_addc_u32 s55, s55, 0
	s_add_u32 s0, s0, 0x100
	s_addc_u32 s1, s1, 0
	s_cmp_gt_u32 s80, 29

.LBB0_1172:
	s_ashr_i32 s39, s38, 31
	s_lshl_b64 s[4:5], s[38:39], 20
	s_add_u32 s40, s18, s4
	s_addc_u32 s41, s19, s5
	s_and_b64 s[4:5], s[36:37], exec
	s_cselect_b32 s4, s41, s1
	s_cselect_b32 s5, s40, s0
	s_ashr_i32 s35, s34, 31
	s_lshl_b64 s[42:43], s[34:35], 20
	s_add_u32 s42, s16, s42
	s_addc_u32 s43, s17, s43
	s_and_b64 s[48:49], s[36:37], exec
	s_cselect_b32 s35, s43, s47
	s_cselect_b32 s39, s42, s46
	s_add_u32 s76, s46, 0x10000
	s_addc_u32 s77, s47, 0
	s_mov_b32 s78, -2
	v_add_u32_e32 v124, s28, v156
	v_add_u32_e32 v170, s45, v156
	ds_read_b128 v[108:111], v124
	ds_read_b128 v[112:115], v124 offset:1024
	ds_read_b128 v[120:123], v124 offset:2048
	ds_read_b128 v[124:127], v124 offset:3072
	ds_read_b128 v[158:161], v170
	ds_read_b128 v[162:165], v170 offset:1024
	ds_read_b128 v[166:169], v170 offset:2048
	ds_read_b128 v[170:173], v170 offset:3072
	s_add_u32 s46, s0, 0x10000
	s_addc_u32 s47, s1, 0
	s_cmp_eq_u32 s78, 28
	s_cselect_b32 s52, s5, s46
	s_cselect_b32 s53, s4, s47
	s_cselect_b32 s50, s39, s76
	s_cselect_b32 s51, s35, s77
	s_add_u32 s48, s52, 0x8000
	s_addc_u32 s49, s53, 0
	v_lshl_add_u64 v[206:207], s[0:1], 0, v[152:153]
	s_add_i32 m0, s56, 0xc000
	ds_read_b128 v[174:177], v157
	ds_read_b128 v[178:181], v157 offset:1024
	ds_read_b128 v[182:185], v157 offset:2048
	ds_read_b128 v[186:189], v157 offset:3072
	ds_read_b128 v[190:193], v157 offset:4096
	ds_read_b128 v[194:197], v157 offset:5120
	ds_read_b128 v[198:201], v157 offset:6144
	ds_read_b128 v[202:205], v157 offset:7168
	global_load_lds_dwordx4 v[206:207], off
	v_lshl_add_u64 v[206:207], s[0:1], 0, v[154:155]
	s_add_i32 m0, s56, 0xe000
	s_nop 0
	global_load_lds_dwordx4 v[206:207], off
	s_waitcnt vmcnt(8)
	s_waitcnt lgkmcnt(0)
	s_barrier
	s_setprio 1
	s_waitcnt lgkmcnt(0)
	v_mfma_f32_16x16x32_bf16 v[140:143], v[108:111], v[174:177], 0
	v_mfma_f32_16x16x32_bf16 v[136:139], v[120:123], v[174:177], 0
	v_mfma_f32_16x16x32_bf16 v[116:119], v[108:111], v[182:185], 0
	v_mfma_f32_16x16x32_bf16 v[104:107], v[120:123], v[182:185], 0
	v_mfma_f32_16x16x32_bf16 v[92:95], v[108:111], v[190:193], 0
	v_mfma_f32_16x16x32_bf16 v[88:91], v[120:123], v[190:193], 0
	v_mfma_f32_16x16x32_bf16 v[76:79], v[108:111], v[198:201], 0
	v_mfma_f32_16x16x32_bf16 v[72:75], v[120:123], v[198:201], 0
	v_mfma_f32_16x16x32_bf16 v[140:143], v[112:115], v[178:181], v[140:143]
	v_mfma_f32_16x16x32_bf16 v[136:139], v[124:127], v[178:181], v[136:139]
	v_mfma_f32_16x16x32_bf16 v[116:119], v[112:115], v[186:189], v[116:119]
	v_mfma_f32_16x16x32_bf16 v[104:107], v[124:127], v[186:189], v[104:107]
	v_mfma_f32_16x16x32_bf16 v[92:95], v[112:115], v[194:197], v[92:95]
	v_mfma_f32_16x16x32_bf16 v[88:91], v[124:127], v[194:197], v[88:91]
	v_mfma_f32_16x16x32_bf16 v[76:79], v[112:115], v[202:205], v[76:79]
	v_mfma_f32_16x16x32_bf16 v[72:75], v[124:127], v[202:205], v[72:75]
	s_setprio 0
	s_setprio 1
	v_mfma_f32_16x16x32_bf16 v[132:135], v[158:161], v[174:177], 0
	v_mfma_f32_16x16x32_bf16 v[128:131], v[166:169], v[174:177], 0
	v_mfma_f32_16x16x32_bf16 v[100:103], v[158:161], v[182:185], 0
	v_mfma_f32_16x16x32_bf16 v[96:99], v[166:169], v[182:185], 0
	v_mfma_f32_16x16x32_bf16 v[84:87], v[158:161], v[190:193], 0
	v_mfma_f32_16x16x32_bf16 v[80:83], v[166:169], v[190:193], 0
	v_mfma_f32_16x16x32_bf16 v[68:71], v[158:161], v[198:201], 0
	v_mfma_f32_16x16x32_bf16 v[64:67], v[166:169], v[198:201], 0
	v_mfma_f32_16x16x32_bf16 v[132:135], v[162:165], v[178:181], v[132:135]
	v_mfma_f32_16x16x32_bf16 v[128:131], v[170:173], v[178:181], v[128:131]
	v_mfma_f32_16x16x32_bf16 v[100:103], v[162:165], v[186:189], v[100:103]
	v_mfma_f32_16x16x32_bf16 v[96:99], v[170:173], v[186:189], v[96:99]
	v_mfma_f32_16x16x32_bf16 v[84:87], v[162:165], v[194:197], v[84:87]
	v_mfma_f32_16x16x32_bf16 v[80:83], v[170:173], v[194:197], v[80:83]
	v_mfma_f32_16x16x32_bf16 v[68:71], v[162:165], v[202:205], v[68:71]
	v_mfma_f32_16x16x32_bf16 v[64:67], v[170:173], v[202:205], v[64:67]
	s_setprio 0
	s_barrier
	s_mov_b32 m0, s30
	v_lshl_add_u64 v[206:207], s[50:51], 0, v[146:147]
	s_add_u32 s0, s50, 0x4000
	ds_read_b128 v[174:177], v157 offset:16384
	ds_read_b128 v[178:181], v157 offset:17408
	ds_read_b128 v[182:185], v157 offset:18432
	ds_read_b128 v[186:189], v157 offset:19456
	ds_read_b128 v[190:193], v157 offset:20480
	ds_read_b128 v[194:197], v157 offset:21504
	ds_read_b128 v[198:201], v157 offset:22528
	ds_read_b128 v[202:205], v157 offset:23552
	global_load_lds_dwordx4 v[206:207], off
	v_lshl_add_u64 v[206:207], s[50:51], 0, v[150:151]
	s_mov_b32 m0, s31
	s_addc_u32 s1, s51, 0
	global_load_lds_dwordx4 v[206:207], off
	v_lshl_add_u64 v[206:207], s[0:1], 0, v[146:147]
	s_mov_b32 m0, s54
	s_nop 0
	global_load_lds_dwordx4 v[206:207], off
	v_lshl_add_u64 v[206:207], s[0:1], 0, v[150:151]
	s_mov_b32 m0, s55
	s_nop 0
	global_load_lds_dwordx4 v[206:207], off
	v_lshl_add_u64 v[206:207], s[52:53], 0, v[144:145]
	s_mov_b32 m0, s56
	s_nop 0
	global_load_lds_dwordx4 v[206:207], off
	v_lshl_add_u64 v[206:207], s[52:53], 0, v[148:149]
	s_mov_b32 m0, s57
	s_nop 0
	global_load_lds_dwordx4 v[206:207], off
	s_waitcnt vmcnt(8)
	s_waitcnt lgkmcnt(0)
	s_barrier
	s_setprio 1
	s_waitcnt lgkmcnt(0)
	v_mfma_f32_16x16x32_bf16 v[60:63], v[108:111], v[174:177], 0
	v_mfma_f32_16x16x32_bf16 v[56:59], v[120:123], v[174:177], 0
	v_mfma_f32_16x16x32_bf16 v[44:47], v[108:111], v[182:185], 0
	v_mfma_f32_16x16x32_bf16 v[40:43], v[120:123], v[182:185], 0
	v_mfma_f32_16x16x32_bf16 v[28:31], v[108:111], v[190:193], 0
	v_mfma_f32_16x16x32_bf16 v[24:27], v[120:123], v[190:193], 0
	v_mfma_f32_16x16x32_bf16 v[12:15], v[108:111], v[198:201], 0
	v_mfma_f32_16x16x32_bf16 v[8:11], v[120:123], v[198:201], 0
	v_mfma_f32_16x16x32_bf16 v[60:63], v[112:115], v[178:181], v[60:63]
	v_mfma_f32_16x16x32_bf16 v[56:59], v[124:127], v[178:181], v[56:59]
	v_mfma_f32_16x16x32_bf16 v[44:47], v[112:115], v[186:189], v[44:47]
	v_mfma_f32_16x16x32_bf16 v[40:43], v[124:127], v[186:189], v[40:43]
	v_mfma_f32_16x16x32_bf16 v[28:31], v[112:115], v[194:197], v[28:31]
	v_mfma_f32_16x16x32_bf16 v[24:27], v[124:127], v[194:197], v[24:27]
	v_mfma_f32_16x16x32_bf16 v[12:15], v[112:115], v[202:205], v[12:15]
	v_mfma_f32_16x16x32_bf16 v[8:11], v[124:127], v[202:205], v[8:11]
	s_setprio 0
	s_setprio 1
	v_mfma_f32_16x16x32_bf16 v[52:55], v[158:161], v[174:177], 0
	v_mfma_f32_16x16x32_bf16 v[48:51], v[166:169], v[174:177], 0
	v_mfma_f32_16x16x32_bf16 v[36:39], v[158:161], v[182:185], 0
	v_mfma_f32_16x16x32_bf16 v[32:35], v[166:169], v[182:185], 0
	v_mfma_f32_16x16x32_bf16 v[20:23], v[158:161], v[190:193], 0
	v_mfma_f32_16x16x32_bf16 v[16:19], v[166:169], v[190:193], 0
	v_mfma_f32_16x16x32_bf16 v[4:7], v[158:161], v[198:201], 0
	v_mfma_f32_16x16x32_bf16 v[0:3], v[166:169], v[198:201], 0
	v_mfma_f32_16x16x32_bf16 v[52:55], v[162:165], v[178:181], v[52:55]
	v_mfma_f32_16x16x32_bf16 v[48:51], v[170:173], v[178:181], v[48:51]
	v_mfma_f32_16x16x32_bf16 v[36:39], v[162:165], v[186:189], v[36:39]
	v_mfma_f32_16x16x32_bf16 v[32:35], v[170:173], v[186:189], v[32:35]
	v_mfma_f32_16x16x32_bf16 v[20:23], v[162:165], v[194:197], v[20:23]
	v_mfma_f32_16x16x32_bf16 v[16:19], v[170:173], v[194:197], v[16:19]
	v_mfma_f32_16x16x32_bf16 v[4:7], v[162:165], v[202:205], v[4:7]
	v_mfma_f32_16x16x32_bf16 v[0:3], v[170:173], v[202:205], v[0:3]
	s_setprio 0
	s_barrier
	v_add_u32_e32 v124, s62, v156
	v_add_u32_e32 v170, s67, v156
	ds_read_b128 v[108:111], v124
	ds_read_b128 v[112:115], v124 offset:1024
	ds_read_b128 v[120:123], v124 offset:2048
	ds_read_b128 v[124:127], v124 offset:3072
	ds_read_b128 v[158:161], v170
	ds_read_b128 v[162:165], v170 offset:1024
	ds_read_b128 v[166:169], v170 offset:2048
	ds_read_b128 v[170:173], v170 offset:3072
	s_add_u32 s0, s52, 0x4000
	s_addc_u32 s1, s53, 0
	s_mov_b32 m0, s58
	v_lshl_add_u64 v[206:207], s[0:1], 0, v[144:145]
	ds_read_b128 v[174:177], v157 offset:32768
	ds_read_b128 v[178:181], v157 offset:33792
	ds_read_b128 v[182:185], v157 offset:34816
	ds_read_b128 v[186:189], v157 offset:35840
	ds_read_b128 v[190:193], v157 offset:36864
	ds_read_b128 v[194:197], v157 offset:37888
	ds_read_b128 v[198:201], v157 offset:38912
	ds_read_b128 v[202:205], v157 offset:39936
	global_load_lds_dwordx4 v[206:207], off
	v_lshl_add_u64 v[206:207], s[0:1], 0, v[148:149]
	s_mov_b32 m0, s59
	s_nop 0
	global_load_lds_dwordx4 v[206:207], off
	s_waitcnt vmcnt(8)
	s_waitcnt lgkmcnt(0)
	s_barrier
	s_setprio 1
	s_waitcnt lgkmcnt(0)
	v_mfma_f32_16x16x32_bf16 v[140:143], v[108:111], v[174:177], v[140:143]
	v_mfma_f32_16x16x32_bf16 v[136:139], v[120:123], v[174:177], v[136:139]
	v_mfma_f32_16x16x32_bf16 v[116:119], v[108:111], v[182:185], v[116:119]
	v_mfma_f32_16x16x32_bf16 v[104:107], v[120:123], v[182:185], v[104:107]
	v_mfma_f32_16x16x32_bf16 v[92:95], v[108:111], v[190:193], v[92:95]
	v_mfma_f32_16x16x32_bf16 v[88:91], v[120:123], v[190:193], v[88:91]
	v_mfma_f32_16x16x32_bf16 v[76:79], v[108:111], v[198:201], v[76:79]
	v_mfma_f32_16x16x32_bf16 v[72:75], v[120:123], v[198:201], v[72:75]
	v_mfma_f32_16x16x32_bf16 v[140:143], v[112:115], v[178:181], v[140:143]
	v_mfma_f32_16x16x32_bf16 v[136:139], v[124:127], v[178:181], v[136:139]
	v_mfma_f32_16x16x32_bf16 v[116:119], v[112:115], v[186:189], v[116:119]
	v_mfma_f32_16x16x32_bf16 v[104:107], v[124:127], v[186:189], v[104:107]
	v_mfma_f32_16x16x32_bf16 v[92:95], v[112:115], v[194:197], v[92:95]
	v_mfma_f32_16x16x32_bf16 v[88:91], v[124:127], v[194:197], v[88:91]
	v_mfma_f32_16x16x32_bf16 v[76:79], v[112:115], v[202:205], v[76:79]
	v_mfma_f32_16x16x32_bf16 v[72:75], v[124:127], v[202:205], v[72:75]
	s_setprio 0
	s_setprio 1
	v_mfma_f32_16x16x32_bf16 v[132:135], v[158:161], v[174:177], v[132:135]
	v_mfma_f32_16x16x32_bf16 v[128:131], v[166:169], v[174:177], v[128:131]
	v_mfma_f32_16x16x32_bf16 v[100:103], v[158:161], v[182:185], v[100:103]
	v_mfma_f32_16x16x32_bf16 v[96:99], v[166:169], v[182:185], v[96:99]
	v_mfma_f32_16x16x32_bf16 v[84:87], v[158:161], v[190:193], v[84:87]
	v_mfma_f32_16x16x32_bf16 v[80:83], v[166:169], v[190:193], v[80:83]
	v_mfma_f32_16x16x32_bf16 v[68:71], v[158:161], v[198:201], v[68:71]
	v_mfma_f32_16x16x32_bf16 v[64:67], v[166:169], v[198:201], v[64:67]
	v_mfma_f32_16x16x32_bf16 v[132:135], v[162:165], v[178:181], v[132:135]
	v_mfma_f32_16x16x32_bf16 v[128:131], v[170:173], v[178:181], v[128:131]
	v_mfma_f32_16x16x32_bf16 v[100:103], v[162:165], v[186:189], v[100:103]
	v_mfma_f32_16x16x32_bf16 v[96:99], v[170:173], v[186:189], v[96:99]
	v_mfma_f32_16x16x32_bf16 v[84:87], v[162:165], v[194:197], v[84:87]
	v_mfma_f32_16x16x32_bf16 v[80:83], v[170:173], v[194:197], v[80:83]
	v_mfma_f32_16x16x32_bf16 v[68:71], v[162:165], v[202:205], v[68:71]
	v_mfma_f32_16x16x32_bf16 v[64:67], v[170:173], v[202:205], v[64:67]
	s_setprio 0
	s_barrier
	s_add_u32 s0, s50, 0x8000
	s_addc_u32 s1, s51, 0
	s_mov_b32 m0, s63
	v_lshl_add_u64 v[206:207], s[0:1], 0, v[146:147]
	ds_read_b128 v[174:177], v157 offset:49152
	ds_read_b128 v[178:181], v157 offset:50176
	ds_read_b128 v[182:185], v157 offset:51200
	ds_read_b128 v[186:189], v157 offset:52224
	ds_read_b128 v[190:193], v157 offset:53248
	ds_read_b128 v[194:197], v157 offset:54272
	ds_read_b128 v[198:201], v157 offset:55296
	ds_read_b128 v[202:205], v157 offset:56320
	global_load_lds_dwordx4 v[206:207], off
	v_lshl_add_u64 v[206:207], s[0:1], 0, v[150:151]
	s_add_u32 s0, s50, 0xc000
	s_mov_b32 m0, s64
	s_addc_u32 s1, s51, 0
	global_load_lds_dwordx4 v[206:207], off
	v_lshl_add_u64 v[206:207], s[0:1], 0, v[146:147]
	s_mov_b32 m0, s68
	s_nop 0
	global_load_lds_dwordx4 v[206:207], off
	v_lshl_add_u64 v[206:207], s[0:1], 0, v[150:151]
	s_mov_b32 m0, s69
	s_nop 0
	global_load_lds_dwordx4 v[206:207], off
	v_lshl_add_u64 v[206:207], s[48:49], 0, v[144:145]
	s_mov_b32 m0, s65
	s_nop 0
	global_load_lds_dwordx4 v[206:207], off
	v_lshl_add_u64 v[206:207], s[48:49], 0, v[148:149]
	s_mov_b32 m0, s66
	s_nop 0
	global_load_lds_dwordx4 v[206:207], off
	s_waitcnt vmcnt(8)
	s_waitcnt lgkmcnt(0)
	s_barrier
	s_setprio 1
	s_waitcnt lgkmcnt(0)
	v_mfma_f32_16x16x32_bf16 v[60:63], v[108:111], v[174:177], v[60:63]
	v_mfma_f32_16x16x32_bf16 v[56:59], v[120:123], v[174:177], v[56:59]
	v_mfma_f32_16x16x32_bf16 v[44:47], v[108:111], v[182:185], v[44:47]
	v_mfma_f32_16x16x32_bf16 v[40:43], v[120:123], v[182:185], v[40:43]
	v_mfma_f32_16x16x32_bf16 v[28:31], v[108:111], v[190:193], v[28:31]
	v_mfma_f32_16x16x32_bf16 v[24:27], v[120:123], v[190:193], v[24:27]
	v_mfma_f32_16x16x32_bf16 v[12:15], v[108:111], v[198:201], v[12:15]
	v_mfma_f32_16x16x32_bf16 v[8:11], v[120:123], v[198:201], v[8:11]
	v_mfma_f32_16x16x32_bf16 v[60:63], v[112:115], v[178:181], v[60:63]
	v_mfma_f32_16x16x32_bf16 v[56:59], v[124:127], v[178:181], v[56:59]
	v_mfma_f32_16x16x32_bf16 v[44:47], v[112:115], v[186:189], v[44:47]
	v_mfma_f32_16x16x32_bf16 v[40:43], v[124:127], v[186:189], v[40:43]
	v_mfma_f32_16x16x32_bf16 v[28:31], v[112:115], v[194:197], v[28:31]
	v_mfma_f32_16x16x32_bf16 v[24:27], v[124:127], v[194:197], v[24:27]
	v_mfma_f32_16x16x32_bf16 v[12:15], v[112:115], v[202:205], v[12:15]
	v_mfma_f32_16x16x32_bf16 v[8:11], v[124:127], v[202:205], v[8:11]
	s_setprio 0
	s_setprio 1
	v_mfma_f32_16x16x32_bf16 v[52:55], v[158:161], v[174:177], v[52:55]
	v_mfma_f32_16x16x32_bf16 v[48:51], v[166:169], v[174:177], v[48:51]
	v_mfma_f32_16x16x32_bf16 v[36:39], v[158:161], v[182:185], v[36:39]
	v_mfma_f32_16x16x32_bf16 v[32:35], v[166:169], v[182:185], v[32:35]
	v_mfma_f32_16x16x32_bf16 v[20:23], v[158:161], v[190:193], v[20:23]
	v_mfma_f32_16x16x32_bf16 v[16:19], v[166:169], v[190:193], v[16:19]
	v_mfma_f32_16x16x32_bf16 v[4:7], v[158:161], v[198:201], v[4:7]
	v_mfma_f32_16x16x32_bf16 v[0:3], v[166:169], v[198:201], v[0:3]
	v_mfma_f32_16x16x32_bf16 v[52:55], v[162:165], v[178:181], v[52:55]
	v_mfma_f32_16x16x32_bf16 v[48:51], v[170:173], v[178:181], v[48:51]
	v_mfma_f32_16x16x32_bf16 v[36:39], v[162:165], v[186:189], v[36:39]
	v_mfma_f32_16x16x32_bf16 v[32:35], v[170:173], v[186:189], v[32:35]
	v_mfma_f32_16x16x32_bf16 v[20:23], v[162:165], v[194:197], v[20:23]
	v_mfma_f32_16x16x32_bf16 v[16:19], v[170:173], v[194:197], v[16:19]
	v_mfma_f32_16x16x32_bf16 v[4:7], v[162:165], v[202:205], v[4:7]
	v_mfma_f32_16x16x32_bf16 v[0:3], v[170:173], v[202:205], v[0:3]
	s_setprio 0
	s_barrier
	s_add_i32 s78, s78, 2
	s_add_u32 s76, s76, 0x10000
	s_addc_u32 s77, s77, 0
	s_cmp_gt_u32 s78, 29
	s_mov_b64 s[0:1], s[46:47]

.LBB0_1247:
	s_ashr_i32 s35, s34, 31
	s_lshl_b64 s[4:5], s[34:35], 22
	s_add_u32 s38, s17, s4
	s_addc_u32 s39, s18, s5
	s_and_b64 s[4:5], s[36:37], exec
	s_cselect_b32 s4, s39, s1
	s_cselect_b32 s5, s38, s0
	s_ashr_i32 s25, s24, 31
	s_lshl_b64 s[40:41], s[24:25], 22
	s_add_u32 s40, s19, s40
	s_addc_u32 s41, s28, s41
	s_and_b64 s[46:47], s[36:37], exec
	s_cselect_b32 s25, s41, s45
	s_cselect_b32 s35, s40, s44
	s_add_u32 s74, s44, 0x10000
	s_addc_u32 s75, s45, 0
	s_mov_b32 s76, -2
	v_add_u32_e32 v92, s30, v206
	v_add_u32_e32 v156, s52, v206
	ds_read_b128 v[72:75], v92
	ds_read_b128 v[76:79], v92 offset:1024
	ds_read_b128 v[84:87], v92 offset:2048
	ds_read_b128 v[92:95], v92 offset:3072
	ds_read_b128 v[144:147], v156
	ds_read_b128 v[148:151], v156 offset:1024
	ds_read_b128 v[152:155], v156 offset:2048
	ds_read_b128 v[156:159], v156 offset:3072
	s_add_u32 s44, s0, 0x10000
	s_addc_u32 s45, s1, 0
	s_cmpk_eq_i32 s76, 0x7c
	s_cselect_b32 s50, s5, s44
	s_cselect_b32 s51, s4, s45
	s_cselect_b32 s48, s35, s74
	s_cselect_b32 s49, s25, s75
	s_add_u32 s46, s50, 0x8000
	s_addc_u32 s47, s51, 0
	v_lshl_add_u64 v[204:205], s[0:1], 0, v[180:181]
	s_add_i32 m0, s56, 0xc000
	ds_read_b128 v[160:163], v207
	ds_read_b128 v[164:167], v207 offset:1024
	ds_read_b128 v[168:171], v207 offset:2048
	ds_read_b128 v[184:187], v207 offset:3072
	ds_read_b128 v[188:191], v207 offset:4096
	ds_read_b128 v[192:195], v207 offset:5120
	ds_read_b128 v[196:199], v207 offset:6144
	ds_read_b128 v[200:203], v207 offset:7168
	global_load_lds_dwordx4 v[204:205], off
	v_lshl_add_u64 v[204:205], s[0:1], 0, v[182:183]
	s_add_i32 m0, s56, 0xe000
	s_nop 0
	global_load_lds_dwordx4 v[204:205], off
	s_waitcnt vmcnt(8)
	s_waitcnt lgkmcnt(0)
	s_barrier
	s_setprio 1
	s_waitcnt lgkmcnt(0)
	v_mfma_f32_16x16x32_bf16 v[140:143], v[72:75], v[160:163], 0
	v_mfma_f32_16x16x32_bf16 v[136:139], v[84:87], v[160:163], 0
	v_mfma_f32_16x16x32_bf16 v[124:127], v[72:75], v[168:171], 0
	v_mfma_f32_16x16x32_bf16 v[120:123], v[84:87], v[168:171], 0
	v_mfma_f32_16x16x32_bf16 v[108:111], v[72:75], v[188:191], 0
	v_mfma_f32_16x16x32_bf16 v[104:107], v[84:87], v[188:191], 0
	v_mfma_f32_16x16x32_bf16 v[88:91], v[72:75], v[196:199], 0
	v_mfma_f32_16x16x32_bf16 v[80:83], v[84:87], v[196:199], 0
	v_mfma_f32_16x16x32_bf16 v[140:143], v[76:79], v[164:167], v[140:143]
	v_mfma_f32_16x16x32_bf16 v[136:139], v[92:95], v[164:167], v[136:139]
	v_mfma_f32_16x16x32_bf16 v[124:127], v[76:79], v[184:187], v[124:127]
	v_mfma_f32_16x16x32_bf16 v[120:123], v[92:95], v[184:187], v[120:123]
	v_mfma_f32_16x16x32_bf16 v[108:111], v[76:79], v[192:195], v[108:111]
	v_mfma_f32_16x16x32_bf16 v[104:107], v[92:95], v[192:195], v[104:107]
	v_mfma_f32_16x16x32_bf16 v[88:91], v[76:79], v[200:203], v[88:91]
	v_mfma_f32_16x16x32_bf16 v[80:83], v[92:95], v[200:203], v[80:83]
	s_setprio 0
	s_setprio 1
	v_mfma_f32_16x16x32_bf16 v[132:135], v[144:147], v[160:163], 0
	v_mfma_f32_16x16x32_bf16 v[128:131], v[152:155], v[160:163], 0
	v_mfma_f32_16x16x32_bf16 v[116:119], v[144:147], v[168:171], 0
	v_mfma_f32_16x16x32_bf16 v[112:115], v[152:155], v[168:171], 0
	v_mfma_f32_16x16x32_bf16 v[100:103], v[144:147], v[188:191], 0
	v_mfma_f32_16x16x32_bf16 v[96:99], v[152:155], v[188:191], 0
	v_mfma_f32_16x16x32_bf16 v[68:71], v[144:147], v[196:199], 0
	v_mfma_f32_16x16x32_bf16 v[64:67], v[152:155], v[196:199], 0
	v_mfma_f32_16x16x32_bf16 v[132:135], v[148:151], v[164:167], v[132:135]
	v_mfma_f32_16x16x32_bf16 v[128:131], v[156:159], v[164:167], v[128:131]
	v_mfma_f32_16x16x32_bf16 v[116:119], v[148:151], v[184:187], v[116:119]
	v_mfma_f32_16x16x32_bf16 v[112:115], v[156:159], v[184:187], v[112:115]
	v_mfma_f32_16x16x32_bf16 v[100:103], v[148:151], v[192:195], v[100:103]
	v_mfma_f32_16x16x32_bf16 v[96:99], v[156:159], v[192:195], v[96:99]
	v_mfma_f32_16x16x32_bf16 v[68:71], v[148:151], v[200:203], v[68:71]
	v_mfma_f32_16x16x32_bf16 v[64:67], v[156:159], v[200:203], v[64:67]
	s_setprio 0
	s_barrier
	s_mov_b32 m0, s31
	v_lshl_add_u64 v[204:205], s[48:49], 0, v[174:175]
	s_add_u32 s0, s48, 0x4000
	ds_read_b128 v[160:163], v207 offset:16384
	ds_read_b128 v[164:167], v207 offset:17408
	ds_read_b128 v[168:171], v207 offset:18432
	ds_read_b128 v[184:187], v207 offset:19456
	ds_read_b128 v[188:191], v207 offset:20480
	ds_read_b128 v[192:195], v207 offset:21504
	ds_read_b128 v[196:199], v207 offset:22528
	ds_read_b128 v[200:203], v207 offset:23552
	global_load_lds_dwordx4 v[204:205], off
	v_lshl_add_u64 v[204:205], s[48:49], 0, v[178:179]
	s_mov_b32 m0, s43
	s_addc_u32 s1, s49, 0
	global_load_lds_dwordx4 v[204:205], off
	v_lshl_add_u64 v[204:205], s[0:1], 0, v[174:175]
	s_mov_b32 m0, s53
	s_nop 0
	global_load_lds_dwordx4 v[204:205], off
	v_lshl_add_u64 v[204:205], s[0:1], 0, v[178:179]
	s_mov_b32 m0, s54
	s_nop 0
	global_load_lds_dwordx4 v[204:205], off
	v_lshl_add_u64 v[204:205], s[50:51], 0, v[172:173]
	s_mov_b32 m0, s56
	s_nop 0
	global_load_lds_dwordx4 v[204:205], off
	v_lshl_add_u64 v[204:205], s[50:51], 0, v[176:177]
	s_mov_b32 m0, s57
	s_nop 0
	global_load_lds_dwordx4 v[204:205], off
	s_waitcnt vmcnt(8)
	s_waitcnt lgkmcnt(0)
	s_barrier
	s_setprio 1
	s_waitcnt lgkmcnt(0)
	v_mfma_f32_16x16x32_bf16 v[60:63], v[72:75], v[160:163], 0
	v_mfma_f32_16x16x32_bf16 v[56:59], v[84:87], v[160:163], 0
	v_mfma_f32_16x16x32_bf16 v[44:47], v[72:75], v[168:171], 0
	v_mfma_f32_16x16x32_bf16 v[40:43], v[84:87], v[168:171], 0
	v_mfma_f32_16x16x32_bf16 v[28:31], v[72:75], v[188:191], 0
	v_mfma_f32_16x16x32_bf16 v[24:27], v[84:87], v[188:191], 0
	v_mfma_f32_16x16x32_bf16 v[12:15], v[72:75], v[196:199], 0
	v_mfma_f32_16x16x32_bf16 v[8:11], v[84:87], v[196:199], 0
	v_mfma_f32_16x16x32_bf16 v[60:63], v[76:79], v[164:167], v[60:63]
	v_mfma_f32_16x16x32_bf16 v[56:59], v[92:95], v[164:167], v[56:59]
	v_mfma_f32_16x16x32_bf16 v[44:47], v[76:79], v[184:187], v[44:47]
	v_mfma_f32_16x16x32_bf16 v[40:43], v[92:95], v[184:187], v[40:43]
	v_mfma_f32_16x16x32_bf16 v[28:31], v[76:79], v[192:195], v[28:31]
	v_mfma_f32_16x16x32_bf16 v[24:27], v[92:95], v[192:195], v[24:27]
	v_mfma_f32_16x16x32_bf16 v[12:15], v[76:79], v[200:203], v[12:15]
	v_mfma_f32_16x16x32_bf16 v[8:11], v[92:95], v[200:203], v[8:11]
	s_setprio 0
	s_setprio 1
	v_mfma_f32_16x16x32_bf16 v[52:55], v[144:147], v[160:163], 0
	v_mfma_f32_16x16x32_bf16 v[48:51], v[152:155], v[160:163], 0
	v_mfma_f32_16x16x32_bf16 v[36:39], v[144:147], v[168:171], 0
	v_mfma_f32_16x16x32_bf16 v[32:35], v[152:155], v[168:171], 0
	v_mfma_f32_16x16x32_bf16 v[20:23], v[144:147], v[188:191], 0
	v_mfma_f32_16x16x32_bf16 v[16:19], v[152:155], v[188:191], 0
	v_mfma_f32_16x16x32_bf16 v[4:7], v[144:147], v[196:199], 0
	v_mfma_f32_16x16x32_bf16 v[0:3], v[152:155], v[196:199], 0
	v_mfma_f32_16x16x32_bf16 v[52:55], v[148:151], v[164:167], v[52:55]
	v_mfma_f32_16x16x32_bf16 v[48:51], v[156:159], v[164:167], v[48:51]
	v_mfma_f32_16x16x32_bf16 v[36:39], v[148:151], v[184:187], v[36:39]
	v_mfma_f32_16x16x32_bf16 v[32:35], v[156:159], v[184:187], v[32:35]
	v_mfma_f32_16x16x32_bf16 v[20:23], v[148:151], v[192:195], v[20:23]
	v_mfma_f32_16x16x32_bf16 v[16:19], v[156:159], v[192:195], v[16:19]
	v_mfma_f32_16x16x32_bf16 v[4:7], v[148:151], v[200:203], v[4:7]
	v_mfma_f32_16x16x32_bf16 v[0:3], v[156:159], v[200:203], v[0:3]
	s_setprio 0
	s_barrier
	v_add_u32_e32 v92, s64, v206
	v_add_u32_e32 v156, s69, v206
	ds_read_b128 v[72:75], v92
	ds_read_b128 v[76:79], v92 offset:1024
	ds_read_b128 v[84:87], v92 offset:2048
	ds_read_b128 v[92:95], v92 offset:3072
	ds_read_b128 v[144:147], v156
	ds_read_b128 v[148:151], v156 offset:1024
	ds_read_b128 v[152:155], v156 offset:2048
	ds_read_b128 v[156:159], v156 offset:3072
	s_add_u32 s0, s50, 0x4000
	s_addc_u32 s1, s51, 0
	s_mov_b32 m0, s58
	v_lshl_add_u64 v[204:205], s[0:1], 0, v[172:173]
	ds_read_b128 v[160:163], v207 offset:32768
	ds_read_b128 v[164:167], v207 offset:33792
	ds_read_b128 v[168:171], v207 offset:34816
	ds_read_b128 v[184:187], v207 offset:35840
	ds_read_b128 v[188:191], v207 offset:36864
	ds_read_b128 v[192:195], v207 offset:37888
	ds_read_b128 v[196:199], v207 offset:38912
	ds_read_b128 v[200:203], v207 offset:39936
	global_load_lds_dwordx4 v[204:205], off
	v_lshl_add_u64 v[204:205], s[0:1], 0, v[176:177]
	s_mov_b32 m0, s59
	s_nop 0
	global_load_lds_dwordx4 v[204:205], off
	s_waitcnt vmcnt(8)
	s_waitcnt lgkmcnt(0)
	s_barrier
	s_setprio 1
	s_waitcnt lgkmcnt(0)
	v_mfma_f32_16x16x32_bf16 v[140:143], v[72:75], v[160:163], v[140:143]
	v_mfma_f32_16x16x32_bf16 v[136:139], v[84:87], v[160:163], v[136:139]
	v_mfma_f32_16x16x32_bf16 v[124:127], v[72:75], v[168:171], v[124:127]
	v_mfma_f32_16x16x32_bf16 v[120:123], v[84:87], v[168:171], v[120:123]
	v_mfma_f32_16x16x32_bf16 v[108:111], v[72:75], v[188:191], v[108:111]
	v_mfma_f32_16x16x32_bf16 v[104:107], v[84:87], v[188:191], v[104:107]
	v_mfma_f32_16x16x32_bf16 v[88:91], v[72:75], v[196:199], v[88:91]
	v_mfma_f32_16x16x32_bf16 v[80:83], v[84:87], v[196:199], v[80:83]
	v_mfma_f32_16x16x32_bf16 v[140:143], v[76:79], v[164:167], v[140:143]
	v_mfma_f32_16x16x32_bf16 v[136:139], v[92:95], v[164:167], v[136:139]
	v_mfma_f32_16x16x32_bf16 v[124:127], v[76:79], v[184:187], v[124:127]
	v_mfma_f32_16x16x32_bf16 v[120:123], v[92:95], v[184:187], v[120:123]
	v_mfma_f32_16x16x32_bf16 v[108:111], v[76:79], v[192:195], v[108:111]
	v_mfma_f32_16x16x32_bf16 v[104:107], v[92:95], v[192:195], v[104:107]
	v_mfma_f32_16x16x32_bf16 v[88:91], v[76:79], v[200:203], v[88:91]
	v_mfma_f32_16x16x32_bf16 v[80:83], v[92:95], v[200:203], v[80:83]
	s_setprio 0
	s_setprio 1
	v_mfma_f32_16x16x32_bf16 v[132:135], v[144:147], v[160:163], v[132:135]
	v_mfma_f32_16x16x32_bf16 v[128:131], v[152:155], v[160:163], v[128:131]
	v_mfma_f32_16x16x32_bf16 v[116:119], v[144:147], v[168:171], v[116:119]
	v_mfma_f32_16x16x32_bf16 v[112:115], v[152:155], v[168:171], v[112:115]
	v_mfma_f32_16x16x32_bf16 v[100:103], v[144:147], v[188:191], v[100:103]
	v_mfma_f32_16x16x32_bf16 v[96:99], v[152:155], v[188:191], v[96:99]
	v_mfma_f32_16x16x32_bf16 v[68:71], v[144:147], v[196:199], v[68:71]
	v_mfma_f32_16x16x32_bf16 v[64:67], v[152:155], v[196:199], v[64:67]
	v_mfma_f32_16x16x32_bf16 v[132:135], v[148:151], v[164:167], v[132:135]
	v_mfma_f32_16x16x32_bf16 v[128:131], v[156:159], v[164:167], v[128:131]
	v_mfma_f32_16x16x32_bf16 v[116:119], v[148:151], v[184:187], v[116:119]
	v_mfma_f32_16x16x32_bf16 v[112:115], v[156:159], v[184:187], v[112:115]
	v_mfma_f32_16x16x32_bf16 v[100:103], v[148:151], v[192:195], v[100:103]
	v_mfma_f32_16x16x32_bf16 v[96:99], v[156:159], v[192:195], v[96:99]
	v_mfma_f32_16x16x32_bf16 v[68:71], v[148:151], v[200:203], v[68:71]
	v_mfma_f32_16x16x32_bf16 v[64:67], v[156:159], v[200:203], v[64:67]
	s_setprio 0
	s_barrier
	s_add_u32 s0, s48, 0x8000
	s_addc_u32 s1, s49, 0
	s_mov_b32 m0, s65
	v_lshl_add_u64 v[204:205], s[0:1], 0, v[174:175]
	ds_read_b128 v[160:163], v207 offset:49152
	ds_read_b128 v[164:167], v207 offset:50176
	ds_read_b128 v[168:171], v207 offset:51200
	ds_read_b128 v[184:187], v207 offset:52224
	ds_read_b128 v[188:191], v207 offset:53248
	ds_read_b128 v[192:195], v207 offset:54272
	ds_read_b128 v[196:199], v207 offset:55296
	ds_read_b128 v[200:203], v207 offset:56320
	global_load_lds_dwordx4 v[204:205], off
	v_lshl_add_u64 v[204:205], s[0:1], 0, v[178:179]
	s_add_u32 s0, s48, 0xc000
	s_mov_b32 m0, s66
	s_addc_u32 s1, s49, 0
	global_load_lds_dwordx4 v[204:205], off
	v_lshl_add_u64 v[204:205], s[0:1], 0, v[174:175]
	s_mov_b32 m0, s70
	s_nop 0
	global_load_lds_dwordx4 v[204:205], off
	v_lshl_add_u64 v[204:205], s[0:1], 0, v[178:179]
	s_mov_b32 m0, s71
	s_nop 0
	global_load_lds_dwordx4 v[204:205], off
	v_lshl_add_u64 v[204:205], s[46:47], 0, v[172:173]
	s_mov_b32 m0, s67
	s_nop 0
	global_load_lds_dwordx4 v[204:205], off
	v_lshl_add_u64 v[204:205], s[46:47], 0, v[176:177]
	s_mov_b32 m0, s68
	s_nop 0
	global_load_lds_dwordx4 v[204:205], off
	s_waitcnt vmcnt(8)
	s_waitcnt lgkmcnt(0)
	s_barrier
	s_setprio 1
	s_waitcnt lgkmcnt(0)
	v_mfma_f32_16x16x32_bf16 v[60:63], v[72:75], v[160:163], v[60:63]
	v_mfma_f32_16x16x32_bf16 v[56:59], v[84:87], v[160:163], v[56:59]
	v_mfma_f32_16x16x32_bf16 v[44:47], v[72:75], v[168:171], v[44:47]
	v_mfma_f32_16x16x32_bf16 v[40:43], v[84:87], v[168:171], v[40:43]
	v_mfma_f32_16x16x32_bf16 v[28:31], v[72:75], v[188:191], v[28:31]
	v_mfma_f32_16x16x32_bf16 v[24:27], v[84:87], v[188:191], v[24:27]
	v_mfma_f32_16x16x32_bf16 v[12:15], v[72:75], v[196:199], v[12:15]
	v_mfma_f32_16x16x32_bf16 v[8:11], v[84:87], v[196:199], v[8:11]
	v_mfma_f32_16x16x32_bf16 v[60:63], v[76:79], v[164:167], v[60:63]
	v_mfma_f32_16x16x32_bf16 v[56:59], v[92:95], v[164:167], v[56:59]
	v_mfma_f32_16x16x32_bf16 v[44:47], v[76:79], v[184:187], v[44:47]
	v_mfma_f32_16x16x32_bf16 v[40:43], v[92:95], v[184:187], v[40:43]
	v_mfma_f32_16x16x32_bf16 v[28:31], v[76:79], v[192:195], v[28:31]
	v_mfma_f32_16x16x32_bf16 v[24:27], v[92:95], v[192:195], v[24:27]
	v_mfma_f32_16x16x32_bf16 v[12:15], v[76:79], v[200:203], v[12:15]
	v_mfma_f32_16x16x32_bf16 v[8:11], v[92:95], v[200:203], v[8:11]
	s_setprio 0
	s_setprio 1
	v_mfma_f32_16x16x32_bf16 v[52:55], v[144:147], v[160:163], v[52:55]
	v_mfma_f32_16x16x32_bf16 v[48:51], v[152:155], v[160:163], v[48:51]
	v_mfma_f32_16x16x32_bf16 v[36:39], v[144:147], v[168:171], v[36:39]
	v_mfma_f32_16x16x32_bf16 v[32:35], v[152:155], v[168:171], v[32:35]
	v_mfma_f32_16x16x32_bf16 v[20:23], v[144:147], v[188:191], v[20:23]
	v_mfma_f32_16x16x32_bf16 v[16:19], v[152:155], v[188:191], v[16:19]
	v_mfma_f32_16x16x32_bf16 v[4:7], v[144:147], v[196:199], v[4:7]
	v_mfma_f32_16x16x32_bf16 v[0:3], v[152:155], v[196:199], v[0:3]
	v_mfma_f32_16x16x32_bf16 v[52:55], v[148:151], v[164:167], v[52:55]
	v_mfma_f32_16x16x32_bf16 v[48:51], v[156:159], v[164:167], v[48:51]
	v_mfma_f32_16x16x32_bf16 v[36:39], v[148:151], v[184:187], v[36:39]
	v_mfma_f32_16x16x32_bf16 v[32:35], v[156:159], v[184:187], v[32:35]
	v_mfma_f32_16x16x32_bf16 v[20:23], v[148:151], v[192:195], v[20:23]
	v_mfma_f32_16x16x32_bf16 v[16:19], v[156:159], v[192:195], v[16:19]
	v_mfma_f32_16x16x32_bf16 v[4:7], v[148:151], v[200:203], v[4:7]
	v_mfma_f32_16x16x32_bf16 v[0:3], v[156:159], v[200:203], v[0:3]
	s_setprio 0
	s_barrier
	s_add_i32 s76, s76, 2
	s_add_u32 s74, s74, 0x10000
	s_addc_u32 s75, s75, 0
	s_cmpk_gt_u32 s76, 0x7d
	s_mov_b64 s[0:1], s[44:45]
